# variant of v28: keep_v29_deep_nt012
# baseline (speedup 1.0000x reference)
.LBB8_5:
	v_add_u32_e32 v22, s18, v47
	v_mov_b32_e32 v23, s14
	v_cmp_gt_u32_e32 vcc, s12, v22
	s_waitcnt lgkmcnt(0)
	s_barrier
	v_add_u32_e32 v56, -4, v46
	v_min_u32_e32 v56, s16, v56
	v_cndmask_b32_e32 v22, v23, v22, vcc
	v_lshlrev_b32_e32 v27, 4, v22
	global_load_dwordx4 v[22:25], v27, s[10:11]
	global_load_dwordx4 v[52:55], v27, s[10:11]
	v_subrev_u32_e32 v27, 52, v46
	v_min_u32_e32 v27, s16, v27
	global_load_dword v27, v27, s[8:9]
	global_load_dword v92, v56, s[8:9]
	v_subrev_u32_e32 v56, 48, v46
	v_min_u32_e32 v56, s17, v56
	global_load_dword v93, v56, s[8:9]
	v_min_u32_e32 v56, s17, v46
	global_load_dword v94, v56, s[8:9]
	v_subrev_u32_e32 v56, 56, v46
	v_min_u32_e32 v56, s15, v56
	global_load_dword v95, v56, s[8:9]
	v_add_u32_e32 v56, -8, v46
	s_add_i32 s25, s24, s19
	v_min_u32_e32 v56, s15, v56
	global_load_dword v96, v56, s[8:9]
	v_lshl_or_b32 v50, v50, 8, v29
	s_add_i32 m0, s25, 0x4000
	s_add_i32 s24, s24, s20
	global_load_lds_dwordx4 v50, s[4:5]
	v_lshl_or_b32 v50, v51, 8, v31
	s_add_i32 m0, s24, 0x4000
	s_add_i32 s2, s2, s3
	global_load_lds_dwordx4 v50, s[4:5]
	v_or_b32_e32 v50, s23, v32
	v_or_b32_e32 v51, s23, v33
	v_or_b32_e32 v97, s23, v34
	v_or_b32_e32 v98, s23, v35
	ds_read_b128 v[56:59], v50 offset:0
	ds_read_b128 v[60:63], v50 offset:0x1000
	ds_read_b128 v[64:67], v50 offset:0x2000
	ds_read_b128 v[68:71], v50 offset:0x3000
	ds_read_b128 v[72:75], v51 offset:0
	s_nop 0
	s_waitcnt lgkmcnt(4)
	s_nop 0
	v_mfma_f32_16x16x32_f16 v[56:59], v[14:17], v[56:59], 0
	ds_read_b128 v[76:79], v51 offset:0x1000
	s_waitcnt lgkmcnt(4)
	s_nop 0
	v_mfma_f32_16x16x32_f16 v[60:63], v[14:17], v[60:63], 0
	ds_read_b128 v[80:83], v51 offset:0x2000
	s_waitcnt lgkmcnt(4)
	s_nop 0
	v_mfma_f32_16x16x32_f16 v[64:67], v[14:17], v[64:67], 0
	ds_read_b128 v[84:87], v51 offset:0x3000
	s_waitcnt lgkmcnt(4)
	s_nop 0
	v_mfma_f32_16x16x32_f16 v[68:71], v[14:17], v[68:71], 0
	ds_read_b128 v[88:91], v97 offset:0
	s_waitcnt lgkmcnt(4)
	s_nop 0
	v_mfma_f32_16x16x32_f16 v[56:59], v[2:5], v[72:75], v[56:59]
	ds_read_b128 v[72:75], v97 offset:0x1000
	s_waitcnt lgkmcnt(4)
	s_nop 0
	v_mfma_f32_16x16x32_f16 v[60:63], v[2:5], v[76:79], v[60:63]
	ds_read_b128 v[76:79], v97 offset:0x2000
	s_waitcnt lgkmcnt(4)
	s_nop 0
	v_mfma_f32_16x16x32_f16 v[64:67], v[2:5], v[80:83], v[64:67]
	ds_read_b128 v[80:83], v97 offset:0x3000
	s_waitcnt lgkmcnt(4)
	s_nop 0
	v_mfma_f32_16x16x32_f16 v[68:71], v[2:5], v[84:87], v[68:71]
	ds_read_b128 v[84:87], v98 offset:0
	s_waitcnt lgkmcnt(4)
	s_nop 0
	v_mfma_f32_16x16x32_f16 v[56:59], v[6:9], v[88:91], v[56:59]
	ds_read_b128 v[88:91], v98 offset:0x1000
	s_waitcnt lgkmcnt(4)
	s_nop 0
	v_mfma_f32_16x16x32_f16 v[60:63], v[6:9], v[72:75], v[60:63]
	ds_read_b128 v[72:75], v98 offset:0x2000
	s_waitcnt lgkmcnt(4)
	s_nop 0
	v_mfma_f32_16x16x32_f16 v[64:67], v[6:9], v[76:79], v[64:67]
	ds_read_b128 v[76:79], v98 offset:0x3000
	s_waitcnt lgkmcnt(4)
	s_nop 0
	v_mfma_f32_16x16x32_f16 v[68:71], v[6:9], v[80:83], v[68:71]
	ds_read_b128 v[80:83], v37 offset:0
	s_waitcnt lgkmcnt(4)
	s_nop 0
	v_mfma_f32_16x16x32_f16 v[56:59], v[10:13], v[84:87], v[56:59]
	ds_read_b128 v[84:87], v37 offset:0x100
	s_waitcnt lgkmcnt(4)
	s_nop 0
	v_mfma_f32_16x16x32_f16 v[60:63], v[10:13], v[88:91], v[60:63]
	ds_read_b128 v[88:91], v37 offset:0x200
	s_waitcnt lgkmcnt(4)
	s_nop 0
	v_mfma_f32_16x16x32_f16 v[64:67], v[10:13], v[72:75], v[64:67]
	ds_read_b128 v[72:75], v37 offset:0x300
	s_waitcnt lgkmcnt(4)
	s_nop 0
	v_mfma_f32_16x16x32_f16 v[68:71], v[10:13], v[76:79], v[68:71]
	s_waitcnt lgkmcnt(3)
	s_nop 0
	v_mfma_f32_16x16x32_f16 v[56:59], v[18:21], v[80:83], v[56:59]
	s_waitcnt lgkmcnt(2)
	s_nop 0
	v_mfma_f32_16x16x32_f16 v[60:63], v[18:21], v[84:87], v[60:63]
	s_waitcnt lgkmcnt(1)
	s_nop 0
	v_mfma_f32_16x16x32_f16 v[64:67], v[18:21], v[88:91], v[64:67]
	s_waitcnt lgkmcnt(0)
	s_nop 0
	v_mfma_f32_16x16x32_f16 v[68:71], v[18:21], v[72:75], v[68:71]
	s_nop 1
	v_max_i32_e32 v50, 0, v56
	v_max_i32_e32 v56, 0, v57
	v_max_i32_e32 v51, 0, v58
	v_max_i32_e32 v57, 0, v59
	v_cvt_pk_f16_f32 v51, v51, v57
	v_cvt_pk_f16_f32 v50, v50, v56
	v_max_i32_e32 v56, 0, v60
	v_max_i32_e32 v58, 0, v61
	v_max_i32_e32 v57, 0, v62
	v_max_i32_e32 v59, 0, v63
	v_cvt_pk_f16_f32 v57, v57, v59
	v_cvt_pk_f16_f32 v56, v56, v58
	ds_write2st64_b64 v48, v[50:51], v[56:57] offset1:8
	v_max_i32_e32 v50, 0, v64
	v_max_i32_e32 v56, 0, v65
	v_max_i32_e32 v51, 0, v66
	v_max_i32_e32 v57, 0, v67
	v_cvt_pk_f16_f32 v51, v51, v57
	v_cvt_pk_f16_f32 v50, v50, v56
	v_max_i32_e32 v56, 0, v68
	v_max_i32_e32 v58, 0, v69
	v_max_i32_e32 v57, 0, v70
	v_max_i32_e32 v59, 0, v71
	v_cvt_pk_f16_f32 v57, v57, v59
	v_cvt_pk_f16_f32 v56, v56, v58
	ds_write2st64_b64 v48, v[50:51], v[56:57] offset0:16 offset1:24
	s_waitcnt lgkmcnt(0)
	s_barrier
	v_lshl_or_b32 v40, v40, 8, v29
	s_add_i32 m0, s25, 0x8000
	s_xor_b64 s[6:7], s[6:7], -1
	global_load_lds_dwordx4 v40, s[4:5]
	v_lshl_or_b32 v40, v41, 8, v31
	s_add_i32 m0, s24, 0x8000
	v_add_u32_e32 v46, s22, v46
	global_load_lds_dwordx4 v40, s[4:5]
	v_lshl_or_b32 v40, v42, 8, v29
	s_mov_b32 m0, s25
	s_nop 0
	global_load_lds_dwordx4 v40, s[4:5]
	v_lshl_or_b32 v40, v45, 8, v31
	s_mov_b32 m0, s24
	s_nop 0
	global_load_lds_dwordx4 v40, s[4:5]
	v_add_u32_e32 v40, v39, v43
	ds_read_b128 v[56:59], v40
	ds_read_b128 v[60:63], v49
	v_add_u32_e32 v40, s18, v38
	v_ashrrev_i32_e32 v41, 31, v40
	v_lshlrev_b64 v[50:51], 8, v[40:41]
	v_add_u32_e32 v40, 32, v40
	v_ashrrev_i32_e32 v41, 31, v40
	v_lshlrev_b64 v[40:41], 8, v[40:41]
	v_lshl_add_u64 v[50:51], v[0:1], 0, v[50:51]
	v_lshl_add_u64 v[40:41], v[0:1], 0, v[40:41]
	s_waitcnt lgkmcnt(0)
	global_store_dwordx4 v[50:51], v[56:59], off nt
	global_store_dwordx4 v[40:41], v[60:63], off nt
	s_add_i32 s18, s18, s21
	s_waitcnt vmcnt(8)
	s_cmp_lt_i32 s2, s13
	v_mov_b32_e32 v50, v27
	v_mov_b32_e32 v51, v92
	v_mov_b32_e32 v40, v93
	v_mov_b32_e32 v41, v94
	v_mov_b32_e32 v42, v95
	v_mov_b32_e32 v45, v96
	s_cbranch_scc0 .LBB8_8
